# NORM2 router: the 8 per-wave partial logits are read from LDS together before summing (one wait instead of 7 dependent round trips per element)
# speedup vs baseline: 1.0071x; 1.0004x over previous
.LBB0_1123:
	ds_read2st64_b32 v[128:129], v127 offset1:8
	ds_read2st64_b32 v[130:131], v127 offset0:24 offset1:32
	ds_read2st64_b32 v[132:133], v127 offset0:48 offset1:56
	ds_read2st64_b32 v[134:135], v127 offset0:72 offset1:80
	ds_read2st64_b32 v[136:137], v127 offset0:96 offset1:104
	ds_read2st64_b32 v[138:139], v127 offset0:120 offset1:128
	ds_read2st64_b32 v[140:141], v127 offset0:144 offset1:152
	ds_read2st64_b32 v[142:143], v127 offset0:168 offset1:176
	v_add_u32_e32 v126, -2, v126
	v_cmp_eq_u32_e32 vcc, 0, v126
	s_or_b64 s[0:1], vcc, s[0:1]
	s_waitcnt lgkmcnt(0)
	v_pk_add_f32 v[128:129], v[128:129], 0 op_sel_hi:[1,0]
	s_waitcnt lgkmcnt(0)
	v_pk_add_f32 v[128:129], v[128:129], v[130:131]
	v_pk_add_f32 v[128:129], v[128:129], v[132:133]
	v_pk_add_f32 v[128:129], v[128:129], v[134:135]
	v_pk_add_f32 v[128:129], v[128:129], v[136:137]
	v_pk_add_f32 v[128:129], v[128:129], v[138:139]
	v_pk_add_f32 v[128:129], v[128:129], v[140:141]
	v_pk_add_f32 v[128:129], v[128:129], v[142:143]
	ds_write2st64_b32 v127, v128, v129 offset0:192 offset1:200
	v_add_u32_e32 v127, 0x1000, v127
	s_andn2_b64 exec, exec, s[0:1]
	s_cbranch_execnz .LBB0_1123
	s_or_b64 exec, exec, s[0:1]
	s_mov_b64 s[0:1], 0
	s_and_saveexec_b64 s[48:49], s[44:45]
	s_mov_b64 s[0:1], exec
	v_lshlrev_b32_e32 v127, 2, v183
	s_or_b64 exec, exec, s[48:49]
	s_orn2_b64 s[0:1], s[0:1], exec
	v_mov_b32_e32 v126, v183

.LBB0_1129:
	ds_read2st64_b32 v[128:129], v127 offset1:24
	ds_read2st64_b32 v[132:133], v127 offset0:48 offset1:72
	ds_read2st64_b32 v[134:135], v127 offset0:96 offset1:120
	ds_read2st64_b32 v[136:137], v127 offset0:144 offset1:168
	v_add_u32_e32 v126, 0x200, v126
	s_movk_i32 s14, 0x3ff
	v_cmp_lt_i32_e32 vcc, s14, v126
	s_or_b64 s[0:1], vcc, s[0:1]
	s_waitcnt lgkmcnt(0)
	v_add_f32_e32 v128, 0, v128
	v_add_f32_e32 v130, v128, v129
	v_add_f32_e32 v128, v130, v132
	v_add_f32_e32 v130, v128, v133
	v_add_f32_e32 v128, v130, v134
	v_add_f32_e32 v130, v128, v135
	v_add_f32_e32 v128, v130, v136
	v_add_f32_e32 v128, v128, v137
	ds_write_b32 v127, v128 offset:49152
	v_add_u32_e32 v127, 0x800, v127
	s_andn2_b64 exec, exec, s[0:1]
	s_cbranch_execnz .LBB0_1129
